# de-serialisation (strategy 2) in ml_out: the 16 g_out gain loads per pass (each followed by vmcnt(0)) issued as 12+4 into dead registers, one wait per batch; on top of v47
# speedup vs baseline: 1.0138x; 1.0065x over previous
.LBB0_726:
	v_or_b32_e32 v7, s49, v203
	v_cmp_gt_i32_e64 s[76:77], s44, v7
	s_waitcnt vmcnt(0)
	global_load_dword v146, v[194:195], off
	global_load_dword v147, v[194:195], off offset:64
	global_load_dword v148, v[194:195], off offset:128
	global_load_dword v149, v[194:195], off offset:192
	global_load_dword v150, v[194:195], off offset:256
	global_load_dword v151, v[194:195], off offset:320
	global_load_dword v152, v[194:195], off offset:384
	global_load_dword v153, v[194:195], off offset:448
	global_load_dword v154, v[194:195], off offset:512
	global_load_dword v155, v[194:195], off offset:576
	global_load_dword v156, v[194:195], off offset:640
	global_load_dword v157, v[194:195], off offset:704
	v_mov_b32_e32 v32, 0
	v_add_u32_e32 v50, s43, v7
	v_lshlrev_b32_e32 v40, 1, v162
	v_mov_b32_e32 v36, 0
	v_mov_b32_e32 v37, 0
	v_mov_b32_e32 v38, 0
	v_mov_b32_e32 v39, 0
	s_and_saveexec_b64 s[70:71], s[76:77]
	s_cbranch_execz .LBB0_728
	v_mov_b64_e32 v[8:9], s[82:83]
	v_mad_i64_i32 v[8:9], s[72:73], v50, s16, v[8:9]
	v_lshl_add_u64 v[8:9], s[6:7], 1, v[8:9]
	v_mov_b32_e32 v41, v6
	v_lshl_add_u64 v[8:9], v[8:9], 0, v[40:41]
	v_add_co_u32_e32 v8, vcc, 0x1000, v8
	s_nop 1
	v_addc_co_u32_e32 v9, vcc, 0, v9, vcc
	global_load_dwordx4 v[36:39], v[8:9], off

.LBB0_742:
	s_or_b64 exec, exec, s[80:81]
	ds_bpermute_b32 v41, v241, v120
	ds_bpermute_b32 v40, v241, v119
	ds_bpermute_b32 v7, v241, v118
	v_mov_b32_e32 v42, v114
	v_mov_b32_e32 v43, v94
	s_waitcnt lgkmcnt(2)
	v_max_f32_e64 v41, |v41|, |v41|
	v_max_f32_e32 v45, 1.0, v41
	ds_bpermute_b32 v41, v241, v121
	s_waitcnt lgkmcnt(2)
	v_max_f32_e64 v40, |v40|, |v40|
	v_max_f32_e32 v40, 1.0, v40
	s_waitcnt lgkmcnt(1)
	v_max_f32_e64 v7, |v7|, |v7|
	v_max_f32_e32 v7, 1.0, v7
	s_waitcnt lgkmcnt(0)
	v_max_f32_e64 v41, |v41|, |v41|
	v_max_f32_e32 v47, 1.0, v41
	v_div_scale_f32 v41, s[80:81], v40, v40, 1.0
	v_rcp_f32_e32 v49, v41
	v_mov_b32_e32 v94, v115
	s_waitcnt lgkmcnt(0)
	s_barrier
	v_fma_f32 v51, -v41, v49, 1.0
	v_fmac_f32_e32 v49, v51, v49
	v_div_scale_f32 v51, vcc, 1.0, v40, 1.0
	v_mul_f32_e32 v52, v51, v49
	v_fma_f32 v53, -v41, v52, v51
	v_fmac_f32_e32 v52, v53, v49
	v_fma_f32 v41, -v41, v52, v51
	v_div_fmas_f32 v41, v41, v49, v52
	v_div_fixup_f32 v53, v41, v40, 1.0
	v_div_scale_f32 v40, s[80:81], v7, v7, 1.0
	v_rcp_f32_e32 v41, v40
	s_nop 0
	v_fma_f32 v49, -v40, v41, 1.0
	v_fmac_f32_e32 v41, v49, v41
	v_div_scale_f32 v49, vcc, 1.0, v7, 1.0
	v_mul_f32_e32 v51, v49, v41
	v_fma_f32 v52, -v40, v51, v49
	v_fmac_f32_e32 v51, v52, v41
	v_fma_f32 v40, -v40, v51, v49
	v_div_fmas_f32 v40, v40, v41, v51
	v_div_fixup_f32 v52, v40, v7, 1.0
	v_div_scale_f32 v7, s[80:81], v47, v47, 1.0
	v_pk_mul_f32 v[122:123], v[74:75], v[52:53]
	v_pk_mul_f32 v[74:75], v[42:43], v[52:53] op_sel_hi:[1,0]
	v_rcp_f32_e32 v42, v7
	v_pk_mul_f32 v[128:129], v[62:63], v[52:53]
	v_pk_mul_f32 v[132:133], v[54:55], v[52:53]
	v_pk_mul_f32 v[40:41], v[128:129], v[128:129]
	v_fma_f32 v43, -v7, v42, 1.0
	v_fmac_f32_e32 v42, v43, v42
	v_div_scale_f32 v43, vcc, 1.0, v47, 1.0
	v_mul_f32_e32 v49, v43, v42
	v_fma_f32 v51, -v7, v49, v43
	v_fmac_f32_e32 v49, v51, v42
	v_fma_f32 v7, -v7, v49, v43
	v_div_fmas_f32 v7, v7, v42, v49
	v_div_fixup_f32 v143, v7, v47, 1.0
	v_div_scale_f32 v7, s[80:81], v45, v45, 1.0
	v_rcp_f32_e32 v42, v7
	v_pk_fma_f32 v[40:41], v[132:133], v[132:133], v[40:41]
	v_pk_mul_f32 v[124:125], v[58:59], v[52:53]
	v_pk_mul_f32 v[120:121], v[70:71], v[52:53]
	v_fma_f32 v43, -v7, v42, 1.0
	v_fmac_f32_e32 v42, v43, v42
	v_div_scale_f32 v43, vcc, 1.0, v45, 1.0
	v_mul_f32_e32 v47, v43, v42
	v_fma_f32 v49, -v7, v47, v43
	v_pk_fma_f32 v[40:41], v[124:125], v[124:125], v[40:41]
	v_fmac_f32_e32 v47, v49, v42
	v_pk_fma_f32 v[40:41], v[122:123], v[122:123], v[40:41]
	v_fma_f32 v7, -v7, v47, v43
	v_pk_fma_f32 v[40:41], v[120:121], v[120:121], v[40:41]
	v_pk_mul_f32 v[118:119], v[66:67], v[52:53]
	v_div_fmas_f32 v7, v7, v42, v47
	v_pk_fma_f32 v[40:41], v[118:119], v[118:119], v[40:41]
	v_pk_mul_f32 v[114:115], v[78:79], v[52:53]
	v_div_fixup_f32 v142, v7, v45, 1.0
	v_pk_fma_f32 v[54:55], v[114:115], v[114:115], v[40:41]
	v_pk_mul_f32 v[40:41], v[90:91], v[52:53]
	v_pk_mul_f32 v[130:131], v[64:65], v[142:143]
	v_pk_fma_f32 v[54:55], v[40:41], v[40:41], v[54:55]
	v_pk_mul_f32 v[86:87], v[86:87], v[52:53]
	v_pk_mul_f32 v[134:135], v[56:57], v[142:143]
	v_pk_mul_f32 v[42:43], v[130:131], v[130:131]
	v_pk_fma_f32 v[54:55], v[86:87], v[86:87], v[54:55]
	v_pk_mul_f32 v[78:79], v[82:83], v[52:53]
	v_pk_fma_f32 v[42:43], v[134:135], v[134:135], v[42:43]
	v_pk_mul_f32 v[126:127], v[60:61], v[142:143]
	v_pk_fma_f32 v[136:137], v[78:79], v[78:79], v[54:55]
	v_mov_b32_e32 v54, v53
	v_mov_b32_e32 v58, v116
	v_mov_b32_e32 v59, v96
	v_mov_b32_e32 v96, v117
	v_pk_fma_f32 v[42:43], v[126:127], v[126:127], v[42:43]
	v_pk_mul_f32 v[116:117], v[76:77], v[142:143]
	v_pk_mul_f32 v[70:71], v[94:95], v[54:55] op_sel_hi:[1,0]
	v_pk_fma_f32 v[42:43], v[116:117], v[116:117], v[42:43]
	v_pk_mul_f32 v[94:95], v[72:73], v[142:143]
	v_pk_mul_f32 v[90:91], v[68:69], v[142:143]
	v_pk_fma_f32 v[42:43], v[94:95], v[94:95], v[42:43]
	v_pk_mul_f32 v[82:83], v[80:81], v[142:143]
	v_pk_fma_f32 v[42:43], v[90:91], v[90:91], v[42:43]
	v_pk_mul_f32 v[80:81], v[88:89], v[142:143]
	v_pk_fma_f32 v[56:57], v[82:83], v[82:83], v[42:43]
	v_pk_mul_f32 v[42:43], v[92:93], v[142:143]
	v_pk_mul_f32 v[76:77], v[84:85], v[142:143]
	v_pk_fma_f32 v[56:57], v[42:43], v[42:43], v[56:57]
	v_pk_mul_f32 v[138:139], v[74:75], v[74:75]
	v_pk_fma_f32 v[56:57], v[80:81], v[80:81], v[56:57]
	v_pk_mul_f32 v[140:141], v[70:71], v[70:71]
	v_pk_fma_f32 v[88:89], v[76:77], v[76:77], v[56:57]
	v_mov_b32_e32 v56, v106
	v_mov_b32_e32 v57, v102
	v_pk_mul_f32 v[62:63], v[56:57], v[52:53] op_sel_hi:[1,0]
	v_mov_b32_e32 v56, v108
	v_mov_b32_e32 v57, v104
	v_pk_mul_f32 v[66:67], v[56:57], v[142:143] op_sel_hi:[1,0]
	v_mov_b32_e32 v56, v110
	v_mov_b32_e32 v57, v98
	v_mov_b32_e32 v84, v143
	v_mov_b32_e32 v102, v107
	v_mov_b32_e32 v104, v109
	v_pk_mul_f32 v[56:57], v[56:57], v[52:53] op_sel_hi:[1,0]
	v_mov_b32_e32 v98, v111
	v_mov_b32_e32 v52, v112
	v_mov_b32_e32 v53, v100
	v_mov_b32_e32 v100, v113
	v_pk_mul_f32 v[72:73], v[58:59], v[142:143] op_sel_hi:[1,0]
	v_pk_mul_f32 v[68:69], v[96:97], v[84:85] op_sel_hi:[1,0]
	v_pk_mul_f32 v[64:65], v[102:103], v[54:55] op_sel_hi:[1,0]
	v_pk_mul_f32 v[60:61], v[104:105], v[84:85] op_sel_hi:[1,0]
	v_pk_mul_f32 v[58:59], v[98:99], v[54:55] op_sel_hi:[1,0]
	v_pk_mul_f32 v[54:55], v[52:53], v[142:143] op_sel_hi:[1,0]
	v_pk_mul_f32 v[52:53], v[100:101], v[84:85] op_sel_hi:[1,0]
	v_mov_b32_e32 v85, v138
	v_mov_b32_e32 v138, v141
	v_pk_mul_f32 v[144:145], v[62:63], v[62:63]
	v_pk_mul_f32 v[102:103], v[64:65], v[64:65]
	v_mov_b32_e32 v84, v140
	v_pk_add_f32 v[112:113], v[138:139], v[136:137] op_sel:[0,1] op_sel_hi:[1,0]
	v_pk_mul_f32 v[108:109], v[56:57], v[56:57]
	v_pk_add_f32 v[84:85], v[84:85], v[112:113]
	v_mov_b32_e32 v112, v103
	v_mov_b32_e32 v113, v145
	v_pk_mul_f32 v[98:99], v[58:59], v[58:59]
	v_pk_add_f32 v[84:85], v[112:113], v[84:85]
	v_mov_b32_e32 v103, v144
	v_pk_add_f32 v[84:85], v[102:103], v[84:85]
	v_mov_b32_e32 v102, v99
	v_mov_b32_e32 v103, v109
	v_pk_add_f32 v[84:85], v[102:103], v[84:85]
	v_mov_b32_e32 v99, v108
	v_pk_add_f32 v[84:85], v[98:99], v[84:85]
	ds_bpermute_b32 v99, v242, v85
	ds_bpermute_b32 v98, v242, v84
	v_pk_mul_f32 v[92:93], v[72:73], v[72:73]
	v_pk_mul_f32 v[96:97], v[68:69], v[68:69]
	v_mov_b32_e32 v103, v92
	v_mov_b32_e32 v92, v97
	s_waitcnt lgkmcnt(0)
	v_pk_add_f32 v[84:85], v[84:85], v[98:99]
	ds_bpermute_b32 v99, v243, v85
	ds_bpermute_b32 v98, v243, v84
	v_pk_mul_f32 v[106:107], v[66:67], v[66:67]
	v_pk_mul_f32 v[104:105], v[60:61], v[60:61]
	v_mov_b32_e32 v102, v96
	v_pk_add_f32 v[88:89], v[92:93], v[88:89] op_sel:[0,1] op_sel_hi:[1,0]
	v_mov_b32_e32 v92, v105
	v_pk_add_f32 v[88:89], v[102:103], v[88:89]
	v_mov_b32_e32 v93, v107
	v_pk_mul_f32 v[110:111], v[54:55], v[54:55]
	v_pk_mul_f32 v[100:101], v[52:53], v[52:53]
	v_pk_add_f32 v[88:89], v[92:93], v[88:89]
	v_mov_b32_e32 v105, v106
	s_waitcnt lgkmcnt(0)
	v_pk_add_f32 v[84:85], v[84:85], v[98:99]
	v_pk_add_f32 v[88:89], v[104:105], v[88:89]
	v_mov_b32_e32 v92, v101
	v_mov_b32_e32 v93, v111
	ds_bpermute_b32 v99, v244, v85
	ds_bpermute_b32 v98, v244, v84
	v_pk_add_f32 v[88:89], v[92:93], v[88:89]
	v_mov_b32_e32 v101, v110
	v_pk_add_f32 v[88:89], v[100:101], v[88:89]
	ds_bpermute_b32 v93, v242, v89
	ds_bpermute_b32 v92, v242, v88
	s_waitcnt lgkmcnt(2)
	v_pk_add_f32 v[84:85], v[84:85], v[98:99]
	ds_bpermute_b32 v99, v245, v85
	ds_bpermute_b32 v98, v245, v84
	s_mov_b32 s80, 0x358637bd
	s_waitcnt lgkmcnt(2)
	v_pk_add_f32 v[88:89], v[88:89], v[92:93]
	ds_bpermute_b32 v93, v243, v89
	ds_bpermute_b32 v92, v243, v88
	s_waitcnt lgkmcnt(2)
	v_pk_add_f32 v[84:85], v[84:85], v[98:99]
	v_mov_b64_e32 v[98:99], s[80:81]
	v_pk_fma_f32 v[84:85], v[84:85], s[8:9], v[98:99] op_sel_hi:[1,0,0]
	s_waitcnt lgkmcnt(0)
	v_pk_add_f32 v[88:89], v[88:89], v[92:93]
	v_mul_f32_e32 v7, 0x4b800000, v85
	v_cmp_gt_f32_e64 s[80:81], s42, v85
	ds_bpermute_b32 v93, v244, v89
	ds_bpermute_b32 v92, v244, v88
	v_cndmask_b32_e64 v7, v85, v7, s[80:81]
	v_rsq_f32_e32 v7, v7
	v_cmp_gt_f32_e32 vcc, s42, v84
	s_waitcnt lgkmcnt(0)
	v_pk_add_f32 v[88:89], v[88:89], v[92:93]
	v_mul_f32_e32 v45, 0x45800000, v7
	v_cndmask_b32_e64 v7, v7, v45, s[80:81]
	v_mul_f32_e32 v45, 0x4b800000, v84
	ds_bpermute_b32 v93, v245, v89
	ds_bpermute_b32 v92, v245, v88
	v_cndmask_b32_e32 v45, v84, v45, vcc
	v_rsq_f32_e32 v45, v45
	v_mul_f32_e32 v40, v40, v7
	s_waitcnt lgkmcnt(0)
	v_pk_add_f32 v[88:89], v[88:89], v[92:93]
	v_mul_f32_e32 v47, 0x45800000, v45
	v_pk_fma_f32 v[88:89], v[88:89], s[8:9], v[98:99] op_sel_hi:[1,0,0]
	v_cndmask_b32_e32 v84, v45, v47, vcc
	v_mul_f32_e32 v45, 0x4b800000, v89
	v_cmp_gt_f32_e64 s[80:81], s42, v89
	v_cmp_gt_f32_e32 vcc, s42, v88
	s_nop 0
	v_cndmask_b32_e64 v45, v89, v45, s[80:81]
	v_rsq_f32_e32 v45, v45
	s_nop 0
	v_mul_f32_e32 v47, 0x45800000, v45
	v_cndmask_b32_e64 v85, v45, v47, s[80:81]
	v_mul_f32_e32 v45, 0x4b800000, v88
	v_cndmask_b32_e32 v45, v88, v45, vcc
	v_rsq_f32_e32 v45, v45
	s_nop 0
	v_mul_f32_e32 v47, 0x45800000, v45
	v_cndmask_b32_e32 v88, v45, v47, vcc
	v_mul_f32_e32 v47, v132, v7
	s_waitcnt vmcnt(0)
	v_mul_f32_e32 v47, v146, v47
	v_bfe_u32 v49, v47, 16, 1
	v_add3_u32 v47, v47, v49, s14
	ds_write_b16_d16_hi v238, v47
	v_mul_f32_e32 v47, v133, v84
	v_mul_f32_e32 v47, v146, v47
	v_bfe_u32 v49, v47, 16, 1
	v_add3_u32 v47, v47, v49, s14
	ds_write_b16_d16_hi v238, v47 offset:272
	v_mul_f32_e32 v47, v134, v85
	v_mul_f32_e32 v47, v146, v47
	v_bfe_u32 v49, v47, 16, 1
	v_add3_u32 v47, v47, v49, s14
	ds_write_b16_d16_hi v238, v47 offset:544
	v_mul_f32_e32 v47, v135, v88
	v_mul_f32_e32 v45, v146, v47
	v_bfe_u32 v47, v45, 16, 1
	v_add3_u32 v45, v45, v47, s14
	ds_write_b16_d16_hi v238, v45 offset:816
	v_mul_f32_e32 v47, v128, v7
	v_mul_f32_e32 v47, v147, v47
	v_bfe_u32 v49, v47, 16, 1
	v_add3_u32 v47, v47, v49, s14
	ds_write_b16_d16_hi v238, v47 offset:32
	v_mul_f32_e32 v47, v129, v84
	v_mul_f32_e32 v47, v147, v47
	v_bfe_u32 v49, v47, 16, 1
	v_add3_u32 v47, v47, v49, s14
	ds_write_b16_d16_hi v238, v47 offset:304
	v_mul_f32_e32 v47, v130, v85
	v_mul_f32_e32 v47, v147, v47
	v_bfe_u32 v49, v47, 16, 1
	v_add3_u32 v47, v47, v49, s14
	ds_write_b16_d16_hi v238, v47 offset:576
	v_mul_f32_e32 v47, v131, v88
	v_mul_f32_e32 v45, v147, v47
	v_bfe_u32 v47, v45, 16, 1
	v_add3_u32 v45, v45, v47, s14
	ds_write_b16_d16_hi v238, v45 offset:848
	v_mul_f32_e32 v47, v124, v7
	v_mul_f32_e32 v47, v148, v47
	v_bfe_u32 v49, v47, 16, 1
	v_add3_u32 v47, v47, v49, s14
	ds_write_b16_d16_hi v238, v47 offset:64
	v_mul_f32_e32 v47, v125, v84
	v_mul_f32_e32 v47, v148, v47
	v_bfe_u32 v49, v47, 16, 1
	v_add3_u32 v47, v47, v49, s14
	ds_write_b16_d16_hi v238, v47 offset:336
	v_mul_f32_e32 v47, v126, v85
	v_mul_f32_e32 v47, v148, v47
	v_bfe_u32 v49, v47, 16, 1
	v_add3_u32 v47, v47, v49, s14
	ds_write_b16_d16_hi v238, v47 offset:608
	v_mul_f32_e32 v47, v127, v88
	v_mul_f32_e32 v45, v148, v47
	v_bfe_u32 v47, v45, 16, 1
	v_add3_u32 v45, v45, v47, s14
	ds_write_b16_d16_hi v238, v45 offset:880
	v_mul_f32_e32 v47, v122, v7
	v_mul_f32_e32 v47, v47, v149
	v_bfe_u32 v49, v47, 16, 1
	v_add3_u32 v47, v47, v49, s14
	ds_write_b16_d16_hi v238, v47 offset:96
	v_mul_f32_e32 v47, v123, v84
	v_mul_f32_e32 v47, v47, v149
	v_bfe_u32 v49, v47, 16, 1
	v_add3_u32 v47, v47, v49, s14
	ds_write_b16_d16_hi v238, v47 offset:368
	v_mul_f32_e32 v47, v116, v85
	v_mul_f32_e32 v47, v149, v47
	v_bfe_u32 v49, v47, 16, 1
	v_add3_u32 v47, v47, v49, s14
	ds_write_b16_d16_hi v238, v47 offset:640
	v_mul_f32_e32 v47, v117, v88
	v_mul_f32_e32 v45, v149, v47
	v_bfe_u32 v47, v45, 16, 1
	v_add3_u32 v45, v45, v47, s14
	ds_write_b16_d16_hi v238, v45 offset:912
	global_load_dword v146, v[194:195], off offset:768
	global_load_dword v147, v[194:195], off offset:832
	global_load_dword v148, v[194:195], off offset:896
	global_load_dword v149, v[194:195], off offset:960
	v_mul_f32_e32 v47, v120, v7
	v_mul_f32_e32 v47, v47, v150
	v_bfe_u32 v49, v47, 16, 1
	v_add3_u32 v47, v47, v49, s14
	ds_write_b16_d16_hi v238, v47 offset:128
	v_mul_f32_e32 v47, v121, v84
	v_mul_f32_e32 v47, v47, v150
	v_bfe_u32 v49, v47, 16, 1
	v_add3_u32 v47, v47, v49, s14
	ds_write_b16_d16_hi v238, v47 offset:400
	v_mul_f32_e32 v47, v94, v85
	v_mul_f32_e32 v47, v47, v150
	v_bfe_u32 v49, v47, 16, 1
	v_add3_u32 v47, v47, v49, s14
	ds_write_b16_d16_hi v238, v47 offset:672
	v_mul_f32_e32 v47, v95, v88
	v_mul_f32_e32 v45, v47, v150
	v_bfe_u32 v47, v45, 16, 1
	v_add3_u32 v45, v45, v47, s14
	ds_write_b16_d16_hi v238, v45 offset:944
	v_mul_f32_e32 v47, v118, v7
	v_mul_f32_e32 v47, v47, v151
	v_bfe_u32 v49, v47, 16, 1
	v_add3_u32 v47, v47, v49, s14
	ds_write_b16_d16_hi v238, v47 offset:160
	v_mul_f32_e32 v47, v119, v84
	v_mul_f32_e32 v47, v47, v151
	v_bfe_u32 v49, v47, 16, 1
	v_add3_u32 v47, v47, v49, s14
	ds_write_b16_d16_hi v238, v47 offset:432
	v_mul_f32_e32 v47, v90, v85
	v_mul_f32_e32 v47, v47, v151
	v_bfe_u32 v49, v47, 16, 1
	v_add3_u32 v47, v47, v49, s14
	ds_write_b16_d16_hi v238, v47 offset:704
	v_mul_f32_e32 v47, v91, v88
	v_mul_f32_e32 v45, v47, v151
	v_bfe_u32 v47, v45, 16, 1
	v_add3_u32 v45, v45, v47, s14
	ds_write_b16_d16_hi v238, v45 offset:976
	v_mul_f32_e32 v47, v114, v7
	v_mul_f32_e32 v47, v47, v152
	v_bfe_u32 v49, v47, 16, 1
	v_add3_u32 v47, v47, v49, s14
	ds_write_b16_d16_hi v238, v47 offset:192
	v_mul_f32_e32 v47, v115, v84
	v_mul_f32_e32 v47, v47, v152
	v_bfe_u32 v49, v47, 16, 1
	v_add3_u32 v47, v47, v49, s14
	ds_write_b16_d16_hi v238, v47 offset:464
	v_mul_f32_e32 v47, v82, v85
	v_mul_f32_e32 v47, v47, v152
	v_bfe_u32 v49, v47, 16, 1
	v_add3_u32 v47, v47, v49, s14
	ds_write_b16_d16_hi v238, v47 offset:736
	v_mul_f32_e32 v47, v83, v88
	v_mul_f32_e32 v45, v47, v152
	v_bfe_u32 v47, v45, 16, 1
	v_add3_u32 v45, v45, v47, s14
	ds_write_b16_d16_hi v238, v45 offset:1008
	v_mul_f32_e32 v40, v40, v153
	v_bfe_u32 v47, v40, 16, 1
	v_add3_u32 v40, v40, v47, s14
	ds_write_b16_d16_hi v238, v40 offset:224
	v_mul_f32_e32 v40, v41, v84
	v_mul_f32_e32 v40, v40, v153
	v_bfe_u32 v41, v40, 16, 1
	v_add3_u32 v40, v40, v41, s14
	ds_write_b16_d16_hi v238, v40 offset:496
	v_mul_f32_e32 v40, v42, v85
	v_mul_f32_e32 v40, v40, v153
	v_bfe_u32 v41, v40, 16, 1
	v_add3_u32 v40, v40, v41, s14
	ds_write_b16_d16_hi v238, v40 offset:768
	v_mul_f32_e32 v40, v43, v88
	v_mul_f32_e32 v40, v40, v153
	v_bfe_u32 v41, v40, 16, 1
	v_add3_u32 v40, v40, v41, s14
	ds_write_b16_d16_hi v238, v40 offset:1040
	s_waitcnt vmcnt(0)
	v_ashrrev_i32_e32 v51, 31, v50
	s_and_saveexec_b64 s[80:81], s[76:77]
	s_cbranch_execz .LBB0_746
	v_lshlrev_b32_e32 v45, 16, v36
	v_mul_f32_e32 v45, 0xbfb8aa3b, v45
	v_exp_f32_e32 v82, v45
	v_lshlrev_b32_e32 v45, 16, v37
	ds_read_b128 v[40:43], v239
	v_mul_f32_e32 v45, 0xbfb8aa3b, v45
	v_exp_f32_e32 v83, v45
	v_and_b32_e32 v36, 0xffff0000, v36
	v_and_b32_e32 v37, 0xffff0000, v37
	s_waitcnt lgkmcnt(0)
	v_lshlrev_b32_e32 v47, 16, v41
	v_pk_add_f32 v[82:83], v[82:83], 1.0 op_sel_hi:[1,0]
	v_lshlrev_b32_e32 v45, 16, v40
	v_rcp_f32_e32 v89, v83
	v_mul_f32_e32 v36, 0xbfb8aa3b, v36
	v_mul_f32_e32 v37, 0xbfb8aa3b, v37
	v_exp_f32_e32 v36, v36
	v_mul_f32_e32 v47, v47, v89
	v_rcp_f32_e32 v83, v82
	v_exp_f32_e32 v37, v37
	v_and_b32_e32 v40, 0xffff0000, v40
	v_and_b32_e32 v41, 0xffff0000, v41
	v_pk_add_f32 v[36:37], v[36:37], 1.0 op_sel_hi:[1,0]
	v_mul_f32_e32 v45, v45, v83
	v_rcp_f32_e32 v82, v36
	s_nop 0
	v_mul_f32_e32 v40, v40, v82
	v_rcp_f32_e32 v49, v37
	s_nop 0
	v_mul_f32_e32 v41, v41, v49
	v_and_b32_e32 v37, 0xffff0000, v38
	v_mul_f32_e32 v37, 0xbfb8aa3b, v37
	v_lshlrev_b32_e32 v36, 16, v38
	v_exp_f32_e32 v38, v37
	v_lshlrev_b32_e32 v37, 16, v39
	v_mul_f32_e32 v36, 0xbfb8aa3b, v36
	v_mul_f32_e32 v37, 0xbfb8aa3b, v37
	v_exp_f32_e32 v36, v36
	v_exp_f32_e32 v37, v37
	v_lshlrev_b32_e32 v82, 16, v43
	v_lshlrev_b32_e32 v49, 16, v42
	v_and_b32_e32 v39, 0xffff0000, v39
	v_pk_add_f32 v[36:37], v[36:37], 1.0 op_sel_hi:[1,0]
	v_mul_f32_e32 v39, 0xbfb8aa3b, v39
	v_rcp_f32_e32 v89, v37
	v_exp_f32_e32 v39, v39
	v_and_b32_e32 v42, 0xffff0000, v42
	v_and_b32_e32 v43, 0xffff0000, v43
	v_mul_f32_e32 v82, v82, v89
	v_rcp_f32_e32 v83, v36
	s_nop 0
	v_mul_f32_e32 v49, v49, v83
	v_pk_add_f32 v[36:37], v[38:39], 1.0 op_sel_hi:[1,0]
	s_nop 0
	v_rcp_f32_e32 v39, v36
	s_nop 0
	v_mul_f32_e32 v36, v42, v39
	v_rcp_f32_e32 v39, v37
	s_nop 0
	v_mul_f32_e32 v37, v43, v39
	v_bfe_u32 v38, v37, 16, 1
	v_bfe_u32 v39, v36, 16, 1
	v_bfe_u32 v42, v41, 16, 1
	v_bfe_u32 v43, v40, 16, 1
	v_add3_u32 v40, v40, v43, s14
	v_add3_u32 v41, v41, v42, s14
	v_add3_u32 v36, v36, v39, s14
	v_add3_u32 v37, v37, v38, s14
	v_bfe_u32 v38, v45, 16, 1
	v_bfe_u32 v39, v47, 16, 1
	v_bfe_u32 v42, v49, 16, 1
	v_bfe_u32 v43, v82, 16, 1
	v_add3_u32 v43, v82, v43, s14
	v_add3_u32 v42, v49, v42, s14
	v_add3_u32 v39, v47, v39, s14
	v_add3_u32 v38, v45, v38, s14
	v_lshrrev_b32_e32 v45, 16, v38
	v_lshrrev_b32_e32 v47, 16, v39
	v_lshrrev_b32_e32 v38, 16, v42
	v_lshrrev_b32_e32 v39, 16, v43
	v_and_or_b32 v39, v37, s17, v39
	v_and_or_b32 v38, v36, s17, v38
	v_and_or_b32 v37, v41, s17, v47
	v_and_or_b32 v36, v40, s17, v45
	v_lshlrev_b64 v[40:41], 11, v[50:51]
	v_lshl_add_u64 v[40:41], v[176:177], 0, v[40:41]
	global_store_dwordx4 v[40:41], v[36:39], off sc1
	s_or_b64 exec, exec, s[80:81]
	v_ashrrev_i32_e32 v49, 31, v48
	s_and_saveexec_b64 s[80:81], s[74:75]
	s_cbranch_execnz .LBB0_747

.LBB0_750:
	s_or_b64 exec, exec, s[80:81]
	s_nop 1
	v_mul_f32_e32 v25, v86, v7
	v_mul_f32_e32 v25, v25, v154
	v_bfe_u32 v26, v25, 16, 1
	v_add3_u32 v25, v25, v26, s14
	ds_write_b16_d16_hi v238, v25
	v_mul_f32_e32 v25, v87, v84
	v_mul_f32_e32 v25, v25, v154
	v_bfe_u32 v26, v25, 16, 1
	v_add3_u32 v25, v25, v26, s14
	ds_write_b16_d16_hi v238, v25 offset:272
	v_mul_f32_e32 v25, v80, v85
	v_mul_f32_e32 v25, v25, v154
	v_bfe_u32 v26, v25, 16, 1
	v_add3_u32 v25, v25, v26, s14
	ds_write_b16_d16_hi v238, v25 offset:544
	v_mul_f32_e32 v25, v81, v88
	v_mul_f32_e32 v24, v25, v154
	v_bfe_u32 v25, v24, 16, 1
	v_add3_u32 v24, v24, v25, s14
	ds_write_b16_d16_hi v238, v24 offset:816
	v_mul_f32_e32 v25, v78, v7
	v_mul_f32_e32 v25, v25, v155
	v_bfe_u32 v26, v25, 16, 1
	v_add3_u32 v25, v25, v26, s14
	ds_write_b16_d16_hi v238, v25 offset:32
	v_mul_f32_e32 v25, v79, v84
	v_mul_f32_e32 v25, v25, v155
	v_bfe_u32 v26, v25, 16, 1
	v_add3_u32 v25, v25, v26, s14
	ds_write_b16_d16_hi v238, v25 offset:304
	v_mul_f32_e32 v25, v76, v85
	v_mul_f32_e32 v25, v25, v155
	v_bfe_u32 v26, v25, 16, 1
	v_add3_u32 v25, v25, v26, s14
	ds_write_b16_d16_hi v238, v25 offset:576
	v_mul_f32_e32 v25, v77, v88
	v_mul_f32_e32 v24, v25, v155
	v_bfe_u32 v25, v24, 16, 1
	v_add3_u32 v24, v24, v25, s14
	ds_write_b16_d16_hi v238, v24 offset:848
	v_mul_f32_e32 v25, v75, v7
	v_mul_f32_e32 v25, v25, v156
	v_bfe_u32 v26, v25, 16, 1
	v_add3_u32 v25, v25, v26, s14
	ds_write_b16_d16_hi v238, v25 offset:64
	v_mul_f32_e32 v25, v71, v84
	v_mul_f32_e32 v25, v25, v156
	v_bfe_u32 v26, v25, 16, 1
	v_add3_u32 v25, v25, v26, s14
	ds_write_b16_d16_hi v238, v25 offset:336
	v_mul_f32_e32 v25, v73, v85
	v_mul_f32_e32 v25, v25, v156
	v_bfe_u32 v26, v25, 16, 1
	v_add3_u32 v25, v25, v26, s14
	ds_write_b16_d16_hi v238, v25 offset:608
	v_mul_f32_e32 v25, v69, v88
	v_mul_f32_e32 v24, v25, v156
	v_bfe_u32 v25, v24, 16, 1
	v_add3_u32 v24, v24, v25, s14
	ds_write_b16_d16_hi v238, v24 offset:880
	v_mul_f32_e32 v25, v74, v7
	v_mul_f32_e32 v25, v25, v157
	v_bfe_u32 v26, v25, 16, 1
	v_add3_u32 v25, v25, v26, s14
	ds_write_b16_d16_hi v238, v25 offset:96
	v_mul_f32_e32 v25, v70, v84
	v_mul_f32_e32 v25, v25, v157
	v_bfe_u32 v26, v25, 16, 1
	v_add3_u32 v25, v25, v26, s14
	ds_write_b16_d16_hi v238, v25 offset:368
	v_mul_f32_e32 v25, v72, v85
	v_mul_f32_e32 v25, v25, v157
	v_bfe_u32 v26, v25, 16, 1
	v_add3_u32 v25, v25, v26, s14
	ds_write_b16_d16_hi v238, v25 offset:640
	v_mul_f32_e32 v25, v68, v88
	v_mul_f32_e32 v24, v25, v157
	v_bfe_u32 v25, v24, 16, 1
	v_add3_u32 v24, v24, v25, s14
	ds_write_b16_d16_hi v238, v24 offset:912
	v_mul_f32_e32 v25, v63, v7
	v_mul_f32_e32 v25, v25, v146
	v_bfe_u32 v26, v25, 16, 1
	v_add3_u32 v25, v25, v26, s14
	ds_write_b16_d16_hi v238, v25 offset:128
	v_mul_f32_e32 v25, v65, v84
	v_mul_f32_e32 v25, v25, v146
	v_bfe_u32 v26, v25, 16, 1
	v_add3_u32 v25, v25, v26, s14
	ds_write_b16_d16_hi v238, v25 offset:400
	v_mul_f32_e32 v25, v67, v85
	v_mul_f32_e32 v25, v25, v146
	v_bfe_u32 v26, v25, 16, 1
	v_add3_u32 v25, v25, v26, s14
	ds_write_b16_d16_hi v238, v25 offset:672
	v_mul_f32_e32 v25, v61, v88
	v_mul_f32_e32 v24, v25, v146
	v_bfe_u32 v25, v24, 16, 1
	v_add3_u32 v24, v24, v25, s14
	ds_write_b16_d16_hi v238, v24 offset:944
	v_mul_f32_e32 v25, v62, v7
	v_mul_f32_e32 v25, v25, v147
	v_bfe_u32 v26, v25, 16, 1
	v_add3_u32 v25, v25, v26, s14
	ds_write_b16_d16_hi v238, v25 offset:160
	v_mul_f32_e32 v25, v64, v84
	v_mul_f32_e32 v25, v25, v147
	v_bfe_u32 v26, v25, 16, 1
	v_add3_u32 v25, v25, v26, s14
	ds_write_b16_d16_hi v238, v25 offset:432
	v_mul_f32_e32 v25, v66, v85
	v_mul_f32_e32 v25, v25, v147
	v_bfe_u32 v26, v25, 16, 1
	v_add3_u32 v25, v25, v26, s14
	ds_write_b16_d16_hi v238, v25 offset:704
	v_mul_f32_e32 v25, v60, v88
	v_mul_f32_e32 v24, v25, v147
	v_bfe_u32 v25, v24, 16, 1
	v_add3_u32 v24, v24, v25, s14
	ds_write_b16_d16_hi v238, v24 offset:976
	v_mul_f32_e32 v25, v57, v7
	v_mul_f32_e32 v7, v56, v7
	v_mul_f32_e32 v25, v25, v148
	v_bfe_u32 v26, v25, 16, 1
	v_add3_u32 v25, v25, v26, s14
	ds_write_b16_d16_hi v238, v25 offset:192
	v_mul_f32_e32 v25, v59, v84
	v_mul_f32_e32 v25, v25, v148
	v_bfe_u32 v26, v25, 16, 1
	v_add3_u32 v25, v25, v26, s14
	ds_write_b16_d16_hi v238, v25 offset:464
	v_mul_f32_e32 v25, v55, v85
	v_mul_f32_e32 v25, v25, v148
	v_bfe_u32 v26, v25, 16, 1
	v_add3_u32 v25, v25, v26, s14
	ds_write_b16_d16_hi v238, v25 offset:736
	v_mul_f32_e32 v25, v53, v88
	v_mul_f32_e32 v24, v25, v148
	v_bfe_u32 v25, v24, 16, 1
	v_add3_u32 v24, v24, v25, s14
	ds_write_b16_d16_hi v238, v24 offset:1008
	v_mul_f32_e32 v7, v7, v149
	v_bfe_u32 v25, v7, 16, 1
	v_add3_u32 v7, v7, v25, s14
	ds_write_b16_d16_hi v238, v7 offset:224
	v_mul_f32_e32 v7, v58, v84
	v_mul_f32_e32 v7, v7, v149
	v_bfe_u32 v25, v7, 16, 1
	v_add3_u32 v7, v7, v25, s14
	ds_write_b16_d16_hi v238, v7 offset:496
	v_mul_f32_e32 v7, v54, v85
	v_mul_f32_e32 v7, v7, v149
	v_bfe_u32 v25, v7, 16, 1
	v_add3_u32 v7, v7, v25, s14
	ds_write_b16_d16_hi v238, v7 offset:768
	v_mul_f32_e32 v7, v52, v88
	v_mul_f32_e32 v7, v7, v149
	v_bfe_u32 v24, v7, 16, 1
	v_add3_u32 v7, v7, v24, s14
	ds_write_b16_d16_hi v238, v7 offset:1040
	s_and_saveexec_b64 s[80:81], s[76:77]
	s_cbranch_execz .LBB0_754
	v_lshlrev_b32_e32 v7, 16, v20
	v_mul_f32_e32 v7, 0xbfb8aa3b, v7
	v_exp_f32_e32 v28, v7
	v_and_b32_e32 v7, 0xffff0000, v20
	v_mul_f32_e32 v7, 0xbfb8aa3b, v7
	v_exp_f32_e32 v20, v7
	v_lshlrev_b32_e32 v7, 16, v21
	ds_read_b128 v[24:27], v239
	v_mul_f32_e32 v7, 0xbfb8aa3b, v7
	v_exp_f32_e32 v29, v7
	v_and_b32_e32 v7, 0xffff0000, v21
	v_mul_f32_e32 v7, 0xbfb8aa3b, v7
	s_waitcnt lgkmcnt(0)
	v_lshlrev_b32_e32 v30, 16, v25
	v_pk_add_f32 v[28:29], v[28:29], 1.0 op_sel_hi:[1,0]
	v_exp_f32_e32 v21, v7
	v_rcp_f32_e32 v32, v29
	v_lshlrev_b32_e32 v7, 16, v24
	v_and_b32_e32 v24, 0xffff0000, v24
	v_pk_add_f32 v[20:21], v[20:21], 1.0 op_sel_hi:[1,0]
	v_mul_f32_e32 v29, v30, v32
	v_rcp_f32_e32 v31, v28
	v_and_b32_e32 v25, 0xffff0000, v25
	v_mul_f32_e32 v7, v7, v31
	v_rcp_f32_e32 v30, v20
	s_nop 0
	v_mul_f32_e32 v24, v24, v30
	v_rcp_f32_e32 v28, v21
	s_nop 0
	v_mul_f32_e32 v25, v25, v28
	v_and_b32_e32 v21, 0xffff0000, v22
	v_mul_f32_e32 v21, 0xbfb8aa3b, v21
	v_lshlrev_b32_e32 v20, 16, v22
	v_exp_f32_e32 v22, v21
	v_lshlrev_b32_e32 v21, 16, v23
	v_mul_f32_e32 v20, 0xbfb8aa3b, v20
	v_mul_f32_e32 v21, 0xbfb8aa3b, v21
	v_exp_f32_e32 v20, v20
	v_exp_f32_e32 v21, v21
	v_lshlrev_b32_e32 v30, 16, v27
	v_lshlrev_b32_e32 v28, 16, v26
	v_and_b32_e32 v23, 0xffff0000, v23
	v_pk_add_f32 v[20:21], v[20:21], 1.0 op_sel_hi:[1,0]
	v_mul_f32_e32 v23, 0xbfb8aa3b, v23
	v_rcp_f32_e32 v32, v21
	v_exp_f32_e32 v23, v23
	v_and_b32_e32 v26, 0xffff0000, v26
	v_and_b32_e32 v27, 0xffff0000, v27
	v_mul_f32_e32 v30, v30, v32
	v_rcp_f32_e32 v31, v20
	s_nop 0
	v_mul_f32_e32 v28, v28, v31
	v_pk_add_f32 v[20:21], v[22:23], 1.0 op_sel_hi:[1,0]
	s_nop 0
	v_rcp_f32_e32 v23, v20
	s_nop 0
	v_mul_f32_e32 v20, v26, v23
	v_rcp_f32_e32 v23, v21
	s_nop 0
	v_mul_f32_e32 v21, v27, v23
	v_bfe_u32 v22, v21, 16, 1
	v_bfe_u32 v23, v20, 16, 1
	v_bfe_u32 v26, v25, 16, 1
	v_bfe_u32 v27, v24, 16, 1
	v_add3_u32 v24, v24, v27, s14
	v_add3_u32 v25, v25, v26, s14
	v_add3_u32 v20, v20, v23, s14
	v_add3_u32 v21, v21, v22, s14
	v_bfe_u32 v22, v7, 16, 1
	v_bfe_u32 v23, v29, 16, 1
	v_bfe_u32 v26, v28, 16, 1
	v_bfe_u32 v27, v30, 16, 1
	v_add3_u32 v27, v30, v27, s14
	v_add3_u32 v26, v28, v26, s14
	v_add3_u32 v23, v29, v23, s14
	v_add3_u32 v7, v7, v22, s14
	v_lshrrev_b32_e32 v7, 16, v7
	v_lshrrev_b32_e32 v28, 16, v23
	v_lshrrev_b32_e32 v22, 16, v26
	v_lshrrev_b32_e32 v23, 16, v27
	v_and_or_b32 v23, v21, s17, v23
	v_and_or_b32 v22, v20, s17, v22
	v_and_or_b32 v21, v25, s17, v28
	v_and_or_b32 v20, v24, s17, v7
	v_lshlrev_b64 v[24:25], 11, v[50:51]
	v_lshl_add_u64 v[24:25], v[176:177], 0, v[24:25]
	global_store_dwordx4 v[24:25], v[20:23], off offset:256 sc1
	s_or_b64 exec, exec, s[80:81]
	s_and_saveexec_b64 s[76:77], s[74:75]
	s_cbranch_execnz .LBB0_755
